# v64 + nt hint on the one-shot f32 weight loads of the P0 weight conversion loops
# speedup vs baseline: 1.0009x; 1.0009x over previous
.LBB0_13:
	s_add_i32 s6, s58, 0xfffff900
	s_cmpk_lt_u32 s6, 0x6000
	s_cbranch_scc1 .LBB0_12
	s_cmpk_gt_i32 s58, 0x4ff
	s_mov_b64 s[2:3], -1
	s_cbranch_scc0 .LBB0_36
	s_cmpk_gt_u32 s58, 0x57f
	s_cbranch_scc0 .LBB0_33
	s_cmpk_gt_u32 s58, 0x5ff
	s_cbranch_scc0 .LBB0_30
	s_cmpk_gt_u32 s58, 0x6ff
	s_cbranch_scc0 .LBB0_27
	s_cmpk_gt_u32 s58, 0x46ff
	s_cbranch_scc0 .LBB0_24
	s_cmpk_gt_u32 s58, 0x66ff
	s_cbranch_scc0 .LBB0_21
	s_add_i32 s0, s58, 0xffff9900
	s_lshr_b32 s0, s0, 5
	s_lshl_b64 s[2:3], s[0:1], 19
	s_lshl_b64 s[60:61], s[0:1], 18
	s_add_u32 s0, s12, s60
	s_addc_u32 s7, s13, s61
	s_and_b32 s33, s16, 0x7c0
	v_or_b32_e32 v4, s33, v105
	v_lshl_add_u64 v[2:3], v[72:73], 0, s[2:3]
	v_lshlrev_b32_e32 v70, 8, v4
	v_lshl_add_u64 v[50:51], v[2:3], 0, v[70:71]
	s_movk_i32 s2, 0x1000
	v_add_co_u32_e32 v30, vcc, s2, v50
	s_movk_i32 s2, 0x2000
	s_nop 0
	v_addc_co_u32_e32 v31, vcc, 0, v51, vcc
	v_add_co_u32_e32 v46, vcc, s2, v50
	s_movk_i32 s2, 0x3000
	s_nop 0
	v_addc_co_u32_e32 v47, vcc, 0, v51, vcc
	v_add_co_u32_e32 v62, vcc, s2, v50
	global_load_dwordx4 v[2:5], v[50:51], off nt
	global_load_dwordx4 v[6:9], v[50:51], off offset:1024 nt
	global_load_dwordx4 v[10:13], v[50:51], off offset:2048 nt
	global_load_dwordx4 v[14:17], v[50:51], off offset:3072 nt
	v_addc_co_u32_e32 v63, vcc, 0, v51, vcc
	global_load_dwordx4 v[18:21], v[46:47], off offset:-4096 nt
	global_load_dwordx4 v[22:25], v[30:31], off offset:1024 nt
	global_load_dwordx4 v[26:29], v[30:31], off offset:2048 nt
	s_nop 0
	global_load_dwordx4 v[30:33], v[30:31], off offset:3072 nt
	s_nop 0
	global_load_dwordx4 v[34:37], v[46:47], off nt
	global_load_dwordx4 v[38:41], v[46:47], off offset:1024 nt
	global_load_dwordx4 v[42:45], v[46:47], off offset:2048 nt
	s_nop 0
	global_load_dwordx4 v[46:49], v[46:47], off offset:3072 nt
	s_nop 0
	global_load_dwordx4 v[50:53], v[62:63], off nt
	global_load_dwordx4 v[54:57], v[62:63], off offset:1024 nt
	global_load_dwordx4 v[58:61], v[62:63], off offset:2048 nt
	s_nop 0
	global_load_dwordx4 v[62:65], v[62:63], off offset:3072 nt
	s_lshl_b32 s2, s33, 1
	s_add_u32 s2, s0, s2
	s_addc_u32 s3, s7, 0
	v_mov_b32_e32 v101, v71
	s_waitcnt vmcnt(14)
	ds_write2_b32 v106, v2, v6 offset1:4
	ds_write2_b32 v106, v3, v7 offset0:65 offset1:69
	ds_write2_b32 v106, v4, v8 offset0:130 offset1:134
	ds_write2_b32 v106, v5, v9 offset0:195 offset1:199
	s_waitcnt vmcnt(12)
	ds_write2_b32 v106, v10, v14 offset0:8 offset1:12
	ds_write2_b32 v106, v11, v15 offset0:73 offset1:77
	ds_write2_b32 v106, v12, v16 offset0:138 offset1:142
	ds_write2_b32 v106, v13, v17 offset0:203 offset1:207
	s_waitcnt vmcnt(10)
	ds_write2_b32 v106, v18, v22 offset0:16 offset1:20
	ds_write2_b32 v106, v19, v23 offset0:81 offset1:85
	ds_write2_b32 v106, v20, v24 offset0:146 offset1:150
	ds_write2_b32 v106, v21, v25 offset0:211 offset1:215
	s_waitcnt vmcnt(8)
	ds_write2_b32 v106, v26, v30 offset0:24 offset1:28
	ds_write2_b32 v106, v27, v31 offset0:89 offset1:93
	ds_write2_b32 v106, v28, v32 offset0:154 offset1:158
	ds_write2_b32 v106, v29, v33 offset0:219 offset1:223
	s_waitcnt vmcnt(6)
	ds_write2_b32 v106, v34, v38 offset0:32 offset1:36
	ds_write2_b32 v106, v35, v39 offset0:97 offset1:101
	ds_write2_b32 v106, v36, v40 offset0:162 offset1:166
	ds_write2_b32 v106, v37, v41 offset0:227 offset1:231
	s_waitcnt vmcnt(4)
	ds_write2_b32 v106, v42, v46 offset0:40 offset1:44
	ds_write2_b32 v106, v43, v47 offset0:105 offset1:109
	ds_write2_b32 v106, v44, v48 offset0:170 offset1:174
	ds_write2_b32 v106, v45, v49 offset0:235 offset1:239
	s_waitcnt vmcnt(2)
	ds_write2_b32 v106, v50, v54 offset0:48 offset1:52
	ds_write2_b32 v106, v51, v55 offset0:113 offset1:117
	ds_write2_b32 v106, v52, v56 offset0:178 offset1:182
	ds_write2_b32 v106, v53, v57 offset0:243 offset1:247
	s_waitcnt vmcnt(0)
	ds_write2_b32 v106, v58, v62 offset0:56 offset1:60
	ds_write2_b32 v106, v59, v63 offset0:121 offset1:125
	ds_write2_b32 v106, v60, v64 offset0:186 offset1:190
	ds_write2_b32 v106, v61, v65 offset0:251 offset1:255
	s_waitcnt lgkmcnt(0)
	ds_read2_b32 v[2:3], v118 offset1:1
	ds_read2_b32 v[4:5], v118 offset0:2 offset1:3
	ds_read2_b32 v[8:9], v118 offset0:6 offset1:7
	v_lshl_add_u64 v[6:7], s[2:3], 0, v[100:101]
	s_mov_b64 s[2:3], 0
	s_waitcnt lgkmcnt(2)
	v_cvt_pk_bf16_f32 v2, v2, v3
	s_waitcnt lgkmcnt(1)
	v_cvt_pk_bf16_f32 v3, v4, v5
	ds_read2_b32 v[4:5], v118 offset0:4 offset1:5
	s_waitcnt lgkmcnt(0)
	v_cvt_pk_bf16_f32 v4, v4, v5
	v_cvt_pk_bf16_f32 v5, v8, v9
	v_lshl_add_u64 v[8:9], v[6:7], 0, v[74:75]
	global_store_dwordx4 v[8:9], v[2:5], off
	ds_read2_b32 v[2:3], v119 offset1:1
	ds_read2_b32 v[4:5], v120 offset1:1
	ds_read2_b32 v[8:9], v122 offset1:1
	s_waitcnt lgkmcnt(2)
	v_cvt_pk_bf16_f32 v2, v2, v3
	s_waitcnt lgkmcnt(1)
	v_cvt_pk_bf16_f32 v3, v4, v5
	ds_read2_b32 v[4:5], v121 offset1:1
	s_waitcnt lgkmcnt(0)
	v_cvt_pk_bf16_f32 v4, v4, v5
	v_cvt_pk_bf16_f32 v5, v8, v9
	v_lshl_add_u64 v[8:9], v[6:7], 0, v[76:77]
	global_store_dwordx4 v[8:9], v[2:5], off
	ds_read2_b32 v[2:3], v123 offset1:1
	ds_read2_b32 v[4:5], v124 offset1:1
	s_waitcnt lgkmcnt(1)
	v_cvt_pk_bf16_f32 v2, v2, v3
	s_waitcnt lgkmcnt(0)
	v_cvt_pk_bf16_f32 v3, v4, v5
	ds_read2_b32 v[4:5], v125 offset1:1
	s_waitcnt lgkmcnt(0)
	v_cvt_pk_bf16_f32 v4, v4, v5
	v_add_u32_e32 v5, 0x1058, v118
	ds_read2_b32 v[8:9], v5 offset1:1
	s_waitcnt lgkmcnt(0)
	v_cvt_pk_bf16_f32 v5, v8, v9
	v_lshl_add_u64 v[8:9], v[6:7], 0, v[78:79]
	global_store_dwordx4 v[8:9], v[2:5], off
	s_nop 1
	v_add_u32_e32 v2, 0x1860, v118
	ds_read2_b32 v[2:3], v2 offset1:1
	s_waitcnt lgkmcnt(0)
	v_cvt_pk_bf16_f32 v2, v2, v3
	v_add_u32_e32 v3, 0x1868, v118
	ds_read2_b32 v[4:5], v3 offset1:1
	s_waitcnt lgkmcnt(0)
	v_cvt_pk_bf16_f32 v3, v4, v5
	v_add_u32_e32 v4, 0x1870, v118
	ds_read2_b32 v[4:5], v4 offset1:1
	s_waitcnt lgkmcnt(0)
	v_cvt_pk_bf16_f32 v4, v4, v5
	v_add_u32_e32 v5, 0x1878, v118
	ds_read2_b32 v[8:9], v5 offset1:1
	s_waitcnt lgkmcnt(0)
	v_cvt_pk_bf16_f32 v5, v8, v9
	v_lshl_add_u64 v[8:9], v[6:7], 0, v[80:81]
	global_store_dwordx4 v[8:9], v[2:5], off
	s_nop 1
	v_add_u32_e32 v2, 0x2080, v118
	ds_read2_b32 v[2:3], v2 offset1:1
	s_waitcnt lgkmcnt(0)
	v_cvt_pk_bf16_f32 v2, v2, v3
	v_add_u32_e32 v3, 0x2088, v118
	ds_read2_b32 v[4:5], v3 offset1:1
	s_waitcnt lgkmcnt(0)
	v_cvt_pk_bf16_f32 v3, v4, v5
	v_add_u32_e32 v4, 0x2090, v118
	ds_read2_b32 v[4:5], v4 offset1:1
	s_waitcnt lgkmcnt(0)
	v_cvt_pk_bf16_f32 v4, v4, v5
	v_add_u32_e32 v5, 0x2098, v118
	ds_read2_b32 v[8:9], v5 offset1:1
	s_waitcnt lgkmcnt(0)
	v_cvt_pk_bf16_f32 v5, v8, v9
	v_lshl_add_u64 v[8:9], v[6:7], 0, v[82:83]
	global_store_dwordx4 v[8:9], v[2:5], off
	s_nop 1
	v_add_u32_e32 v2, 0x28a0, v118
	ds_read2_b32 v[2:3], v2 offset1:1
	s_waitcnt lgkmcnt(0)
	v_cvt_pk_bf16_f32 v2, v2, v3
	v_add_u32_e32 v3, 0x28a8, v118
	ds_read2_b32 v[4:5], v3 offset1:1
	s_waitcnt lgkmcnt(0)
	v_cvt_pk_bf16_f32 v3, v4, v5
	v_add_u32_e32 v4, 0x28b0, v118
	ds_read2_b32 v[4:5], v4 offset1:1
	s_waitcnt lgkmcnt(0)
	v_cvt_pk_bf16_f32 v4, v4, v5
	v_add_u32_e32 v5, 0x28b8, v118
	ds_read2_b32 v[8:9], v5 offset1:1
	s_waitcnt lgkmcnt(0)
	v_cvt_pk_bf16_f32 v5, v8, v9
	v_lshl_add_u64 v[8:9], v[6:7], 0, v[84:85]
	global_store_dwordx4 v[8:9], v[2:5], off
	s_nop 1
	v_add_u32_e32 v2, 0x30c0, v118
	ds_read2_b32 v[2:3], v2 offset1:1
	s_waitcnt lgkmcnt(0)
	v_cvt_pk_bf16_f32 v2, v2, v3
	v_add_u32_e32 v3, 0x30c8, v118
	ds_read2_b32 v[4:5], v3 offset1:1
	s_waitcnt lgkmcnt(0)
	v_cvt_pk_bf16_f32 v3, v4, v5
	v_add_u32_e32 v4, 0x30d0, v118
	ds_read2_b32 v[4:5], v4 offset1:1
	s_waitcnt lgkmcnt(0)
	v_cvt_pk_bf16_f32 v4, v4, v5
	v_add_u32_e32 v5, 0x30d8, v118
	ds_read2_b32 v[8:9], v5 offset1:1
	s_waitcnt lgkmcnt(0)
	v_cvt_pk_bf16_f32 v5, v8, v9
	v_lshl_add_u64 v[8:9], v[6:7], 0, v[86:87]
	global_store_dwordx4 v[8:9], v[2:5], off
	v_lshl_add_u64 v[6:7], v[6:7], 0, v[88:89]
	s_nop 0
	v_add_u32_e32 v2, 0x38e0, v118
	ds_read2_b32 v[2:3], v2 offset1:1
	s_waitcnt lgkmcnt(0)
	v_cvt_pk_bf16_f32 v2, v2, v3
	v_add_u32_e32 v3, 0x38e8, v118
	ds_read2_b32 v[4:5], v3 offset1:1
	s_waitcnt lgkmcnt(0)
	v_cvt_pk_bf16_f32 v3, v4, v5
	v_add_u32_e32 v4, 0x38f0, v118
	ds_read2_b32 v[4:5], v4 offset1:1
	s_waitcnt lgkmcnt(0)
	v_cvt_pk_bf16_f32 v4, v4, v5
	v_add_u32_e32 v5, 0x38f8, v118
	ds_read2_b32 v[8:9], v5 offset1:1
	s_waitcnt lgkmcnt(0)
	v_cvt_pk_bf16_f32 v5, v8, v9
	global_store_dwordx4 v[6:7], v[2:5], off
	s_waitcnt lgkmcnt(0)

.LBB0_27:
	s_andn2_b64 vcc, exec, s[2:3]
	s_cbranch_vccnz .LBB0_29
	s_and_b32 s0, s18, 0x1fc0
	s_and_b32 s2, s16, 0x3c0
	s_addk_i32 s0, 0xe800
	v_or_b32_e32 v2, s2, v67
	v_readlane_b32 s60, v255, 3
	v_or_b32_e32 v58, s0, v105
	v_lshlrev_b32_e32 v70, 2, v2
	v_readlane_b32 s64, v255, 7
	v_readlane_b32 s65, v255, 8
	v_mov_b32_e32 v59, v71
	v_lshlrev_b64 v[2:3], 12, v[58:59]
	v_lshl_add_u64 v[60:61], s[64:65], 0, v[70:71]
	v_or_b32_e32 v70, 4, v58
	v_lshlrev_b64 v[4:5], 12, v[70:71]
	v_or_b32_e32 v70, 8, v58
	v_lshlrev_b64 v[10:11], 12, v[70:71]
	v_or_b32_e32 v70, 12, v58
	v_lshlrev_b64 v[12:13], 12, v[70:71]
	v_or_b32_e32 v70, 16, v58
	v_lshlrev_b64 v[18:19], 12, v[70:71]
	v_or_b32_e32 v70, 20, v58
	v_lshlrev_b64 v[20:21], 12, v[70:71]
	v_or_b32_e32 v70, 24, v58
	v_lshlrev_b64 v[26:27], 12, v[70:71]
	v_or_b32_e32 v70, 28, v58
	v_lshlrev_b64 v[28:29], 12, v[70:71]
	v_or_b32_e32 v70, 32, v58
	v_lshlrev_b64 v[34:35], 12, v[70:71]
	v_or_b32_e32 v70, 36, v58
	v_lshlrev_b64 v[36:37], 12, v[70:71]
	v_or_b32_e32 v70, 40, v58
	v_lshlrev_b64 v[42:43], 12, v[70:71]
	v_or_b32_e32 v70, 44, v58
	v_lshlrev_b64 v[44:45], 12, v[70:71]
	v_or_b32_e32 v70, 48, v58
	v_lshlrev_b64 v[50:51], 12, v[70:71]
	v_or_b32_e32 v70, 52, v58
	v_lshlrev_b64 v[52:53], 12, v[70:71]
	v_or_b32_e32 v70, 56, v58
	v_lshlrev_b64 v[62:63], 12, v[70:71]
	v_or_b32_e32 v70, 60, v58
	v_lshlrev_b64 v[58:59], 12, v[70:71]
	v_lshl_add_u64 v[2:3], v[60:61], 0, v[2:3]
	v_lshl_add_u64 v[6:7], v[60:61], 0, v[4:5]
	v_lshl_add_u64 v[10:11], v[60:61], 0, v[10:11]
	v_lshl_add_u64 v[14:15], v[60:61], 0, v[12:13]
	v_lshl_add_u64 v[18:19], v[60:61], 0, v[18:19]
	v_lshl_add_u64 v[22:23], v[60:61], 0, v[20:21]
	v_lshl_add_u64 v[26:27], v[60:61], 0, v[26:27]
	v_lshl_add_u64 v[30:31], v[60:61], 0, v[28:29]
	v_lshl_add_u64 v[34:35], v[60:61], 0, v[34:35]
	v_lshl_add_u64 v[38:39], v[60:61], 0, v[36:37]
	v_lshl_add_u64 v[42:43], v[60:61], 0, v[42:43]
	v_lshl_add_u64 v[46:47], v[60:61], 0, v[44:45]
	v_lshl_add_u64 v[50:51], v[60:61], 0, v[50:51]
	v_lshl_add_u64 v[54:55], v[60:61], 0, v[52:53]
	v_lshl_add_u64 v[62:63], v[60:61], 0, v[62:63]
	v_lshl_add_u64 v[64:65], v[60:61], 0, v[58:59]
	global_load_dwordx4 v[2:5], v[2:3], off nt
	s_nop 0
	global_load_dwordx4 v[6:9], v[6:7], off nt
	s_nop 0
	global_load_dwordx4 v[10:13], v[10:11], off nt
	s_nop 0
	global_load_dwordx4 v[14:17], v[14:15], off nt
	s_nop 0
	global_load_dwordx4 v[18:21], v[18:19], off nt
	s_nop 0
	global_load_dwordx4 v[22:25], v[22:23], off nt
	s_nop 0
	global_load_dwordx4 v[26:29], v[26:27], off nt
	s_nop 0
	global_load_dwordx4 v[30:33], v[30:31], off nt
	s_nop 0
	global_load_dwordx4 v[34:37], v[34:35], off nt
	s_nop 0
	global_load_dwordx4 v[38:41], v[38:39], off nt
	s_nop 0
	global_load_dwordx4 v[42:45], v[42:43], off nt
	s_nop 0
	global_load_dwordx4 v[46:49], v[46:47], off nt
	s_nop 0
	global_load_dwordx4 v[50:53], v[50:51], off nt
	s_nop 0
	global_load_dwordx4 v[54:57], v[54:55], off nt
	s_nop 0
	global_load_dwordx4 v[58:61], v[62:63], off nt
	s_nop 0
	global_load_dwordx4 v[62:65], v[64:65], off nt
	v_readlane_b32 s61, v255, 4
	v_readlane_b32 s62, v255, 5
	v_readlane_b32 s63, v255, 6
	v_readlane_b32 s66, v255, 9
	v_readlane_b32 s67, v255, 10
	v_readlane_b32 s68, v255, 11
	v_readlane_b32 s69, v255, 12
	v_readlane_b32 s70, v255, 13
	v_readlane_b32 s71, v255, 14
	v_readlane_b32 s72, v255, 15
	v_readlane_b32 s73, v255, 16
	v_readlane_b32 s74, v255, 17
	v_readlane_b32 s75, v255, 18
	s_waitcnt vmcnt(14)
	ds_write2_b32 v106, v2, v6 offset1:4
	ds_write2_b32 v106, v3, v7 offset0:65 offset1:69
	ds_write2_b32 v106, v4, v8 offset0:130 offset1:134
	ds_write2_b32 v106, v5, v9 offset0:195 offset1:199
	s_waitcnt vmcnt(12)
	ds_write2_b32 v106, v10, v14 offset0:8 offset1:12
	ds_write2_b32 v106, v11, v15 offset0:73 offset1:77
	ds_write2_b32 v106, v12, v16 offset0:138 offset1:142
	ds_write2_b32 v106, v13, v17 offset0:203 offset1:207
	s_waitcnt vmcnt(10)
	ds_write2_b32 v106, v18, v22 offset0:16 offset1:20
	ds_write2_b32 v106, v19, v23 offset0:81 offset1:85
	ds_write2_b32 v106, v20, v24 offset0:146 offset1:150
	ds_write2_b32 v106, v21, v25 offset0:211 offset1:215
	s_waitcnt vmcnt(8)
	ds_write2_b32 v106, v26, v30 offset0:24 offset1:28
	ds_write2_b32 v106, v27, v31 offset0:89 offset1:93
	ds_write2_b32 v106, v28, v32 offset0:154 offset1:158
	ds_write2_b32 v106, v29, v33 offset0:219 offset1:223
	s_waitcnt vmcnt(6)
	ds_write2_b32 v106, v34, v38 offset0:32 offset1:36
	ds_write2_b32 v106, v35, v39 offset0:97 offset1:101
	ds_write2_b32 v106, v36, v40 offset0:162 offset1:166
	ds_write2_b32 v106, v37, v41 offset0:227 offset1:231
	s_waitcnt vmcnt(4)
	ds_write2_b32 v106, v42, v46 offset0:40 offset1:44
	ds_write2_b32 v106, v43, v47 offset0:105 offset1:109
	ds_write2_b32 v106, v44, v48 offset0:170 offset1:174
	ds_write2_b32 v106, v45, v49 offset0:235 offset1:239
	s_waitcnt vmcnt(2)
	ds_write2_b32 v106, v50, v54 offset0:48 offset1:52
	ds_write2_b32 v106, v51, v55 offset0:113 offset1:117
	ds_write2_b32 v106, v52, v56 offset0:178 offset1:182
	ds_write2_b32 v106, v53, v57 offset0:243 offset1:247
	s_waitcnt vmcnt(0)
	ds_write2_b32 v106, v58, v62 offset0:56 offset1:60
	ds_write2_b32 v106, v59, v63 offset0:121 offset1:125
	ds_write2_b32 v106, v60, v64 offset0:186 offset1:190
	ds_write2_b32 v106, v61, v65 offset0:251 offset1:255
	s_waitcnt lgkmcnt(0)
	ds_read2_b32 v[2:3], v118 offset1:1
	ds_read2_b32 v[4:5], v118 offset0:2 offset1:3
	ds_read2_b32 v[6:7], v118 offset0:4 offset1:5
	ds_read2_b32 v[8:9], v118 offset0:6 offset1:7
	v_lshl_add_u64 v[10:11], s[0:1], 1, v[92:93]
	s_waitcnt lgkmcnt(3)
	v_cvt_pk_bf16_f32 v2, v2, v3
	s_waitcnt lgkmcnt(2)
	v_cvt_pk_bf16_f32 v3, v4, v5
	s_waitcnt lgkmcnt(1)
	v_cvt_pk_bf16_f32 v4, v6, v7
	s_waitcnt lgkmcnt(0)
	v_cvt_pk_bf16_f32 v5, v8, v9
	ds_read2_b32 v[8:9], v119 offset1:1
	ds_read2_b32 v[12:13], v120 offset1:1
	ds_read2_b32 v[14:15], v121 offset1:1
	ds_read2_b32 v[16:17], v122 offset1:1
	v_or_b32_e32 v6, s2, v107
	v_lshlrev_b32_e32 v70, 11, v6
	v_lshl_add_u64 v[6:7], v[10:11], 0, v[70:71]
	global_store_dwordx4 v[6:7], v[2:5], off
	v_or_b32_e32 v6, s2, v108
	v_lshlrev_b32_e32 v70, 11, v6
	s_waitcnt lgkmcnt(0)
	v_cvt_pk_bf16_f32 v5, v16, v17
	v_add_u32_e32 v16, 0x1058, v118
	v_cvt_pk_bf16_f32 v2, v8, v9
	v_cvt_pk_bf16_f32 v3, v12, v13
	v_cvt_pk_bf16_f32 v4, v14, v15
	ds_read2_b32 v[8:9], v123 offset1:1
	ds_read2_b32 v[12:13], v124 offset1:1
	ds_read2_b32 v[14:15], v125 offset1:1
	ds_read2_b32 v[16:17], v16 offset1:1
	v_lshl_add_u64 v[6:7], v[10:11], 0, v[70:71]
	global_store_dwordx4 v[6:7], v[2:5], off
	v_or_b32_e32 v6, s2, v109
	v_lshlrev_b32_e32 v70, 11, v6
	s_waitcnt lgkmcnt(3)
	v_cvt_pk_bf16_f32 v2, v8, v9
	s_waitcnt lgkmcnt(2)
	v_cvt_pk_bf16_f32 v3, v12, v13
	s_waitcnt lgkmcnt(1)
	v_cvt_pk_bf16_f32 v4, v14, v15
	s_waitcnt lgkmcnt(0)
	v_cvt_pk_bf16_f32 v5, v16, v17
	v_add_u32_e32 v8, 0x1860, v118
	v_add_u32_e32 v12, 0x1868, v118
	v_add_u32_e32 v14, 0x1870, v118
	v_add_u32_e32 v16, 0x1878, v118
	ds_read2_b32 v[8:9], v8 offset1:1
	ds_read2_b32 v[12:13], v12 offset1:1
	ds_read2_b32 v[14:15], v14 offset1:1
	ds_read2_b32 v[16:17], v16 offset1:1
	v_lshl_add_u64 v[6:7], v[10:11], 0, v[70:71]
	global_store_dwordx4 v[6:7], v[2:5], off
	v_or_b32_e32 v6, s2, v110
	v_lshlrev_b32_e32 v70, 11, v6
	s_waitcnt lgkmcnt(3)
	v_cvt_pk_bf16_f32 v2, v8, v9
	s_waitcnt lgkmcnt(2)
	v_cvt_pk_bf16_f32 v3, v12, v13
	s_waitcnt lgkmcnt(1)
	v_cvt_pk_bf16_f32 v4, v14, v15
	s_waitcnt lgkmcnt(0)
	v_cvt_pk_bf16_f32 v5, v16, v17
	v_add_u32_e32 v8, 0x2080, v118
	v_add_u32_e32 v12, 0x2088, v118
	v_add_u32_e32 v14, 0x2090, v118
	v_add_u32_e32 v16, 0x2098, v118
	ds_read2_b32 v[8:9], v8 offset1:1
	ds_read2_b32 v[12:13], v12 offset1:1
	ds_read2_b32 v[14:15], v14 offset1:1
	ds_read2_b32 v[16:17], v16 offset1:1
	v_lshl_add_u64 v[6:7], v[10:11], 0, v[70:71]
	global_store_dwordx4 v[6:7], v[2:5], off
	v_or_b32_e32 v6, s2, v111
	v_lshlrev_b32_e32 v70, 11, v6
	s_waitcnt lgkmcnt(3)
	v_cvt_pk_bf16_f32 v2, v8, v9
	s_waitcnt lgkmcnt(2)
	v_cvt_pk_bf16_f32 v3, v12, v13
	s_waitcnt lgkmcnt(1)
	v_cvt_pk_bf16_f32 v4, v14, v15
	s_waitcnt lgkmcnt(0)
	v_cvt_pk_bf16_f32 v5, v16, v17
	v_add_u32_e32 v8, 0x28a0, v118
	v_add_u32_e32 v12, 0x28a8, v118
	v_add_u32_e32 v14, 0x28b0, v118
	v_add_u32_e32 v16, 0x28b8, v118
	ds_read2_b32 v[8:9], v8 offset1:1
	ds_read2_b32 v[12:13], v12 offset1:1
	ds_read2_b32 v[14:15], v14 offset1:1
	ds_read2_b32 v[16:17], v16 offset1:1
	v_lshl_add_u64 v[6:7], v[10:11], 0, v[70:71]
	global_store_dwordx4 v[6:7], v[2:5], off
	v_or_b32_e32 v6, s2, v112
	v_lshlrev_b32_e32 v70, 11, v6
	s_waitcnt lgkmcnt(3)
	v_cvt_pk_bf16_f32 v2, v8, v9
	s_waitcnt lgkmcnt(2)
	v_cvt_pk_bf16_f32 v3, v12, v13
	s_waitcnt lgkmcnt(1)
	v_cvt_pk_bf16_f32 v4, v14, v15
	s_waitcnt lgkmcnt(0)
	v_cvt_pk_bf16_f32 v5, v16, v17
	v_add_u32_e32 v8, 0x30c0, v118
	v_add_u32_e32 v12, 0x30c8, v118
	v_add_u32_e32 v14, 0x30d0, v118
	v_add_u32_e32 v16, 0x30d8, v118
	ds_read2_b32 v[8:9], v8 offset1:1
	ds_read2_b32 v[12:13], v12 offset1:1
	ds_read2_b32 v[14:15], v14 offset1:1
	ds_read2_b32 v[16:17], v16 offset1:1
	v_lshl_add_u64 v[6:7], v[10:11], 0, v[70:71]
	global_store_dwordx4 v[6:7], v[2:5], off
	v_or_b32_e32 v6, s2, v113
	v_lshlrev_b32_e32 v70, 11, v6
	s_waitcnt lgkmcnt(3)
	v_cvt_pk_bf16_f32 v2, v8, v9
	s_waitcnt lgkmcnt(2)
	v_cvt_pk_bf16_f32 v3, v12, v13
	s_waitcnt lgkmcnt(1)
	v_cvt_pk_bf16_f32 v4, v14, v15
	s_waitcnt lgkmcnt(0)
	v_cvt_pk_bf16_f32 v5, v16, v17
	v_add_u32_e32 v8, 0x38e0, v118
	v_add_u32_e32 v12, 0x38e8, v118
	v_add_u32_e32 v14, 0x38f0, v118
	v_add_u32_e32 v16, 0x38f8, v118
	ds_read2_b32 v[8:9], v8 offset1:1
	ds_read2_b32 v[12:13], v12 offset1:1
	ds_read2_b32 v[14:15], v14 offset1:1
	ds_read2_b32 v[16:17], v16 offset1:1
	v_lshl_add_u64 v[6:7], v[10:11], 0, v[70:71]
	global_store_dwordx4 v[6:7], v[2:5], off
	v_or_b32_e32 v6, s2, v114
	v_lshlrev_b32_e32 v70, 11, v6
	s_waitcnt lgkmcnt(3)
	v_cvt_pk_bf16_f32 v2, v8, v9
	s_waitcnt lgkmcnt(2)
	v_cvt_pk_bf16_f32 v3, v12, v13
	s_waitcnt lgkmcnt(1)
	v_cvt_pk_bf16_f32 v4, v14, v15
	s_waitcnt lgkmcnt(0)
	v_cvt_pk_bf16_f32 v5, v16, v17
	v_lshl_add_u64 v[6:7], v[10:11], 0, v[70:71]
	global_store_dwordx4 v[6:7], v[2:5], off
	s_waitcnt lgkmcnt(0)

.LBB0_30:
	s_andn2_b64 vcc, exec, s[2:3]
	s_cbranch_vccnz .LBB0_32
	s_and_b32 s0, s18, 0x1fc0
	s_and_b32 s2, s16, 0x3c0
	s_addk_i32 s0, 0xea00
	v_or_b32_e32 v2, s2, v67
	v_readlane_b32 s60, v255, 3
	v_or_b32_e32 v58, s0, v105
	v_lshlrev_b32_e32 v70, 2, v2
	v_readlane_b32 s62, v255, 5
	v_readlane_b32 s63, v255, 6
	v_mov_b32_e32 v59, v71
	v_lshlrev_b64 v[2:3], 12, v[58:59]
	v_lshl_add_u64 v[60:61], s[62:63], 0, v[70:71]
	v_or_b32_e32 v70, 4, v58
	v_lshlrev_b64 v[4:5], 12, v[70:71]
	v_or_b32_e32 v70, 8, v58
	v_lshlrev_b64 v[10:11], 12, v[70:71]
	v_or_b32_e32 v70, 12, v58
	v_lshlrev_b64 v[12:13], 12, v[70:71]
	v_or_b32_e32 v70, 16, v58
	v_lshlrev_b64 v[18:19], 12, v[70:71]
	v_or_b32_e32 v70, 20, v58
	v_lshlrev_b64 v[20:21], 12, v[70:71]
	v_or_b32_e32 v70, 24, v58
	v_lshlrev_b64 v[26:27], 12, v[70:71]
	v_or_b32_e32 v70, 28, v58
	v_lshlrev_b64 v[28:29], 12, v[70:71]
	v_or_b32_e32 v70, 32, v58
	v_lshlrev_b64 v[34:35], 12, v[70:71]
	v_or_b32_e32 v70, 36, v58
	v_lshlrev_b64 v[36:37], 12, v[70:71]
	v_or_b32_e32 v70, 40, v58
	v_lshlrev_b64 v[42:43], 12, v[70:71]
	v_or_b32_e32 v70, 44, v58
	v_lshlrev_b64 v[44:45], 12, v[70:71]
	v_or_b32_e32 v70, 48, v58
	v_lshlrev_b64 v[50:51], 12, v[70:71]
	v_or_b32_e32 v70, 52, v58
	v_lshlrev_b64 v[52:53], 12, v[70:71]
	v_or_b32_e32 v70, 56, v58
	v_lshlrev_b64 v[62:63], 12, v[70:71]
	v_or_b32_e32 v70, 60, v58
	v_lshlrev_b64 v[58:59], 12, v[70:71]
	v_lshl_add_u64 v[2:3], v[60:61], 0, v[2:3]
	v_lshl_add_u64 v[6:7], v[60:61], 0, v[4:5]
	v_lshl_add_u64 v[10:11], v[60:61], 0, v[10:11]
	v_lshl_add_u64 v[14:15], v[60:61], 0, v[12:13]
	v_lshl_add_u64 v[18:19], v[60:61], 0, v[18:19]
	v_lshl_add_u64 v[22:23], v[60:61], 0, v[20:21]
	v_lshl_add_u64 v[26:27], v[60:61], 0, v[26:27]
	v_lshl_add_u64 v[30:31], v[60:61], 0, v[28:29]
	v_lshl_add_u64 v[34:35], v[60:61], 0, v[34:35]
	v_lshl_add_u64 v[38:39], v[60:61], 0, v[36:37]
	v_lshl_add_u64 v[42:43], v[60:61], 0, v[42:43]
	v_lshl_add_u64 v[46:47], v[60:61], 0, v[44:45]
	v_lshl_add_u64 v[50:51], v[60:61], 0, v[50:51]
	v_lshl_add_u64 v[54:55], v[60:61], 0, v[52:53]
	v_lshl_add_u64 v[62:63], v[60:61], 0, v[62:63]
	v_lshl_add_u64 v[64:65], v[60:61], 0, v[58:59]
	global_load_dwordx4 v[2:5], v[2:3], off nt
	s_nop 0
	global_load_dwordx4 v[6:9], v[6:7], off nt
	s_nop 0
	global_load_dwordx4 v[10:13], v[10:11], off nt
	s_nop 0
	global_load_dwordx4 v[14:17], v[14:15], off nt
	s_nop 0
	global_load_dwordx4 v[18:21], v[18:19], off nt
	s_nop 0
	global_load_dwordx4 v[22:25], v[22:23], off nt
	s_nop 0
	global_load_dwordx4 v[26:29], v[26:27], off nt
	s_nop 0
	global_load_dwordx4 v[30:33], v[30:31], off nt
	s_nop 0
	global_load_dwordx4 v[34:37], v[34:35], off nt
	s_nop 0
	global_load_dwordx4 v[38:41], v[38:39], off nt
	s_nop 0
	global_load_dwordx4 v[42:45], v[42:43], off nt
	s_nop 0
	global_load_dwordx4 v[46:49], v[46:47], off nt
	s_nop 0
	global_load_dwordx4 v[50:53], v[50:51], off nt
	s_nop 0
	global_load_dwordx4 v[54:57], v[54:55], off nt
	s_nop 0
	global_load_dwordx4 v[58:61], v[62:63], off nt
	s_nop 0
	global_load_dwordx4 v[62:65], v[64:65], off nt
	v_readlane_b32 s61, v255, 4
	v_readlane_b32 s64, v255, 7
	v_readlane_b32 s65, v255, 8
	v_readlane_b32 s66, v255, 9
	v_readlane_b32 s67, v255, 10
	v_readlane_b32 s68, v255, 11
	v_readlane_b32 s69, v255, 12
	v_readlane_b32 s70, v255, 13
	v_readlane_b32 s71, v255, 14
	v_readlane_b32 s72, v255, 15
	v_readlane_b32 s73, v255, 16
	v_readlane_b32 s74, v255, 17
	v_readlane_b32 s75, v255, 18
	s_waitcnt vmcnt(14)
	ds_write2_b32 v106, v2, v6 offset1:4
	ds_write2_b32 v106, v3, v7 offset0:65 offset1:69
	ds_write2_b32 v106, v4, v8 offset0:130 offset1:134
	ds_write2_b32 v106, v5, v9 offset0:195 offset1:199
	s_waitcnt vmcnt(12)
	ds_write2_b32 v106, v10, v14 offset0:8 offset1:12
	ds_write2_b32 v106, v11, v15 offset0:73 offset1:77
	ds_write2_b32 v106, v12, v16 offset0:138 offset1:142
	ds_write2_b32 v106, v13, v17 offset0:203 offset1:207
	s_waitcnt vmcnt(10)
	ds_write2_b32 v106, v18, v22 offset0:16 offset1:20
	ds_write2_b32 v106, v19, v23 offset0:81 offset1:85
	ds_write2_b32 v106, v20, v24 offset0:146 offset1:150
	ds_write2_b32 v106, v21, v25 offset0:211 offset1:215
	s_waitcnt vmcnt(8)
	ds_write2_b32 v106, v26, v30 offset0:24 offset1:28
	ds_write2_b32 v106, v27, v31 offset0:89 offset1:93
	ds_write2_b32 v106, v28, v32 offset0:154 offset1:158
	ds_write2_b32 v106, v29, v33 offset0:219 offset1:223
	s_waitcnt vmcnt(6)
	ds_write2_b32 v106, v34, v38 offset0:32 offset1:36
	ds_write2_b32 v106, v35, v39 offset0:97 offset1:101
	ds_write2_b32 v106, v36, v40 offset0:162 offset1:166
	ds_write2_b32 v106, v37, v41 offset0:227 offset1:231
	s_waitcnt vmcnt(4)
	ds_write2_b32 v106, v42, v46 offset0:40 offset1:44
	ds_write2_b32 v106, v43, v47 offset0:105 offset1:109
	ds_write2_b32 v106, v44, v48 offset0:170 offset1:174
	ds_write2_b32 v106, v45, v49 offset0:235 offset1:239
	s_waitcnt vmcnt(2)
	ds_write2_b32 v106, v50, v54 offset0:48 offset1:52
	ds_write2_b32 v106, v51, v55 offset0:113 offset1:117
	ds_write2_b32 v106, v52, v56 offset0:178 offset1:182
	ds_write2_b32 v106, v53, v57 offset0:243 offset1:247
	s_waitcnt vmcnt(0)
	ds_write2_b32 v106, v58, v62 offset0:56 offset1:60
	ds_write2_b32 v106, v59, v63 offset0:121 offset1:125
	ds_write2_b32 v106, v60, v64 offset0:186 offset1:190
	ds_write2_b32 v106, v61, v65 offset0:251 offset1:255
	s_waitcnt lgkmcnt(0)
	ds_read2_b32 v[2:3], v118 offset1:1
	ds_read2_b32 v[4:5], v118 offset0:2 offset1:3
	ds_read2_b32 v[6:7], v118 offset0:4 offset1:5
	ds_read2_b32 v[8:9], v118 offset0:6 offset1:7
	v_lshl_add_u64 v[10:11], s[0:1], 1, v[94:95]
	s_waitcnt lgkmcnt(3)
	v_cvt_pk_bf16_f32 v2, v2, v3
	s_waitcnt lgkmcnt(2)
	v_cvt_pk_bf16_f32 v3, v4, v5
	s_waitcnt lgkmcnt(1)
	v_cvt_pk_bf16_f32 v4, v6, v7
	s_waitcnt lgkmcnt(0)
	v_cvt_pk_bf16_f32 v5, v8, v9
	ds_read2_b32 v[8:9], v119 offset1:1
	ds_read2_b32 v[12:13], v120 offset1:1
	ds_read2_b32 v[14:15], v121 offset1:1
	ds_read2_b32 v[16:17], v122 offset1:1
	v_or_b32_e32 v6, s2, v107
	v_lshlrev_b32_e32 v70, 11, v6
	v_lshl_add_u64 v[6:7], v[10:11], 0, v[70:71]
	global_store_dwordx4 v[6:7], v[2:5], off
	v_or_b32_e32 v6, s2, v108
	v_lshlrev_b32_e32 v70, 11, v6
	s_waitcnt lgkmcnt(0)
	v_cvt_pk_bf16_f32 v5, v16, v17
	v_add_u32_e32 v16, 0x1058, v118
	v_cvt_pk_bf16_f32 v2, v8, v9
	v_cvt_pk_bf16_f32 v3, v12, v13
	v_cvt_pk_bf16_f32 v4, v14, v15
	ds_read2_b32 v[8:9], v123 offset1:1
	ds_read2_b32 v[12:13], v124 offset1:1
	ds_read2_b32 v[14:15], v125 offset1:1
	ds_read2_b32 v[16:17], v16 offset1:1
	v_lshl_add_u64 v[6:7], v[10:11], 0, v[70:71]
	global_store_dwordx4 v[6:7], v[2:5], off
	v_or_b32_e32 v6, s2, v109
	v_lshlrev_b32_e32 v70, 11, v6
	s_waitcnt lgkmcnt(3)
	v_cvt_pk_bf16_f32 v2, v8, v9
	s_waitcnt lgkmcnt(2)
	v_cvt_pk_bf16_f32 v3, v12, v13
	s_waitcnt lgkmcnt(1)
	v_cvt_pk_bf16_f32 v4, v14, v15
	s_waitcnt lgkmcnt(0)
	v_cvt_pk_bf16_f32 v5, v16, v17
	v_add_u32_e32 v8, 0x1860, v118
	v_add_u32_e32 v12, 0x1868, v118
	v_add_u32_e32 v14, 0x1870, v118
	v_add_u32_e32 v16, 0x1878, v118
	ds_read2_b32 v[8:9], v8 offset1:1
	ds_read2_b32 v[12:13], v12 offset1:1
	ds_read2_b32 v[14:15], v14 offset1:1
	ds_read2_b32 v[16:17], v16 offset1:1
	v_lshl_add_u64 v[6:7], v[10:11], 0, v[70:71]
	global_store_dwordx4 v[6:7], v[2:5], off
	v_or_b32_e32 v6, s2, v110
	v_lshlrev_b32_e32 v70, 11, v6
	s_waitcnt lgkmcnt(3)
	v_cvt_pk_bf16_f32 v2, v8, v9
	s_waitcnt lgkmcnt(2)
	v_cvt_pk_bf16_f32 v3, v12, v13
	s_waitcnt lgkmcnt(1)
	v_cvt_pk_bf16_f32 v4, v14, v15
	s_waitcnt lgkmcnt(0)
	v_cvt_pk_bf16_f32 v5, v16, v17
	v_add_u32_e32 v8, 0x2080, v118
	v_add_u32_e32 v12, 0x2088, v118
	v_add_u32_e32 v14, 0x2090, v118
	v_add_u32_e32 v16, 0x2098, v118
	ds_read2_b32 v[8:9], v8 offset1:1
	ds_read2_b32 v[12:13], v12 offset1:1
	ds_read2_b32 v[14:15], v14 offset1:1
	ds_read2_b32 v[16:17], v16 offset1:1
	v_lshl_add_u64 v[6:7], v[10:11], 0, v[70:71]
	global_store_dwordx4 v[6:7], v[2:5], off
	v_or_b32_e32 v6, s2, v111
	v_lshlrev_b32_e32 v70, 11, v6
	s_waitcnt lgkmcnt(3)
	v_cvt_pk_bf16_f32 v2, v8, v9
	s_waitcnt lgkmcnt(2)
	v_cvt_pk_bf16_f32 v3, v12, v13
	s_waitcnt lgkmcnt(1)
	v_cvt_pk_bf16_f32 v4, v14, v15
	s_waitcnt lgkmcnt(0)
	v_cvt_pk_bf16_f32 v5, v16, v17
	v_add_u32_e32 v8, 0x28a0, v118
	v_add_u32_e32 v12, 0x28a8, v118
	v_add_u32_e32 v14, 0x28b0, v118
	v_add_u32_e32 v16, 0x28b8, v118
	ds_read2_b32 v[8:9], v8 offset1:1
	ds_read2_b32 v[12:13], v12 offset1:1
	ds_read2_b32 v[14:15], v14 offset1:1
	ds_read2_b32 v[16:17], v16 offset1:1
	v_lshl_add_u64 v[6:7], v[10:11], 0, v[70:71]
	global_store_dwordx4 v[6:7], v[2:5], off
	v_or_b32_e32 v6, s2, v112
	v_lshlrev_b32_e32 v70, 11, v6
	s_waitcnt lgkmcnt(3)
	v_cvt_pk_bf16_f32 v2, v8, v9
	s_waitcnt lgkmcnt(2)
	v_cvt_pk_bf16_f32 v3, v12, v13
	s_waitcnt lgkmcnt(1)
	v_cvt_pk_bf16_f32 v4, v14, v15
	s_waitcnt lgkmcnt(0)
	v_cvt_pk_bf16_f32 v5, v16, v17
	v_add_u32_e32 v8, 0x30c0, v118
	v_add_u32_e32 v12, 0x30c8, v118
	v_add_u32_e32 v14, 0x30d0, v118
	v_add_u32_e32 v16, 0x30d8, v118
	ds_read2_b32 v[8:9], v8 offset1:1
	ds_read2_b32 v[12:13], v12 offset1:1
	ds_read2_b32 v[14:15], v14 offset1:1
	ds_read2_b32 v[16:17], v16 offset1:1
	v_lshl_add_u64 v[6:7], v[10:11], 0, v[70:71]
	global_store_dwordx4 v[6:7], v[2:5], off
	v_or_b32_e32 v6, s2, v113
	v_lshlrev_b32_e32 v70, 11, v6
	s_waitcnt lgkmcnt(3)
	v_cvt_pk_bf16_f32 v2, v8, v9
	s_waitcnt lgkmcnt(2)
	v_cvt_pk_bf16_f32 v3, v12, v13
	s_waitcnt lgkmcnt(1)
	v_cvt_pk_bf16_f32 v4, v14, v15
	s_waitcnt lgkmcnt(0)
	v_cvt_pk_bf16_f32 v5, v16, v17
	v_add_u32_e32 v8, 0x38e0, v118
	v_add_u32_e32 v12, 0x38e8, v118
	v_add_u32_e32 v14, 0x38f0, v118
	v_add_u32_e32 v16, 0x38f8, v118
	ds_read2_b32 v[8:9], v8 offset1:1
	ds_read2_b32 v[12:13], v12 offset1:1
	ds_read2_b32 v[14:15], v14 offset1:1
	ds_read2_b32 v[16:17], v16 offset1:1
	v_lshl_add_u64 v[6:7], v[10:11], 0, v[70:71]
	global_store_dwordx4 v[6:7], v[2:5], off
	v_or_b32_e32 v6, s2, v114
	v_lshlrev_b32_e32 v70, 11, v6
	s_waitcnt lgkmcnt(3)
	v_cvt_pk_bf16_f32 v2, v8, v9
	s_waitcnt lgkmcnt(2)
	v_cvt_pk_bf16_f32 v3, v12, v13
	s_waitcnt lgkmcnt(1)
	v_cvt_pk_bf16_f32 v4, v14, v15
	s_waitcnt lgkmcnt(0)
	v_cvt_pk_bf16_f32 v5, v16, v17
	v_lshl_add_u64 v[6:7], v[10:11], 0, v[70:71]
	global_store_dwordx4 v[6:7], v[2:5], off
	s_waitcnt lgkmcnt(0)

.LBB0_33:
	s_andn2_b64 vcc, exec, s[2:3]
	s_cbranch_vccnz .LBB0_35
	s_and_b32 s0, s18, 0x1fc0
	s_and_b32 s2, s16, 0x3c0
	s_addk_i32 s0, 0xec00
	v_or_b32_e32 v2, s2, v67
	v_readlane_b32 s60, v255, 3
	v_or_b32_e32 v58, s0, v105
	v_lshlrev_b32_e32 v70, 2, v2
	v_readlane_b32 s61, v255, 4
	v_mov_b32_e32 v59, v71
	v_lshlrev_b64 v[2:3], 12, v[58:59]
	v_lshl_add_u64 v[60:61], s[60:61], 0, v[70:71]
	v_or_b32_e32 v70, 4, v58
	v_lshlrev_b64 v[4:5], 12, v[70:71]
	v_or_b32_e32 v70, 8, v58
	v_lshlrev_b64 v[10:11], 12, v[70:71]
	v_or_b32_e32 v70, 12, v58
	v_lshlrev_b64 v[12:13], 12, v[70:71]
	v_or_b32_e32 v70, 16, v58
	v_lshlrev_b64 v[18:19], 12, v[70:71]
	v_or_b32_e32 v70, 20, v58
	v_lshlrev_b64 v[20:21], 12, v[70:71]
	v_or_b32_e32 v70, 24, v58
	v_lshlrev_b64 v[26:27], 12, v[70:71]
	v_or_b32_e32 v70, 28, v58
	v_lshlrev_b64 v[28:29], 12, v[70:71]
	v_or_b32_e32 v70, 32, v58
	v_lshlrev_b64 v[34:35], 12, v[70:71]
	v_or_b32_e32 v70, 36, v58
	v_lshlrev_b64 v[36:37], 12, v[70:71]
	v_or_b32_e32 v70, 40, v58
	v_lshlrev_b64 v[42:43], 12, v[70:71]
	v_or_b32_e32 v70, 44, v58
	v_lshlrev_b64 v[44:45], 12, v[70:71]
	v_or_b32_e32 v70, 48, v58
	v_lshlrev_b64 v[50:51], 12, v[70:71]
	v_or_b32_e32 v70, 52, v58
	v_lshlrev_b64 v[52:53], 12, v[70:71]
	v_or_b32_e32 v70, 56, v58
	v_lshlrev_b64 v[62:63], 12, v[70:71]
	v_or_b32_e32 v70, 60, v58
	v_lshlrev_b64 v[58:59], 12, v[70:71]
	v_lshl_add_u64 v[2:3], v[60:61], 0, v[2:3]
	v_lshl_add_u64 v[6:7], v[60:61], 0, v[4:5]
	v_lshl_add_u64 v[10:11], v[60:61], 0, v[10:11]
	v_lshl_add_u64 v[14:15], v[60:61], 0, v[12:13]
	v_lshl_add_u64 v[18:19], v[60:61], 0, v[18:19]
	v_lshl_add_u64 v[22:23], v[60:61], 0, v[20:21]
	v_lshl_add_u64 v[26:27], v[60:61], 0, v[26:27]
	v_lshl_add_u64 v[30:31], v[60:61], 0, v[28:29]
	v_lshl_add_u64 v[34:35], v[60:61], 0, v[34:35]
	v_lshl_add_u64 v[38:39], v[60:61], 0, v[36:37]
	v_lshl_add_u64 v[42:43], v[60:61], 0, v[42:43]
	v_lshl_add_u64 v[46:47], v[60:61], 0, v[44:45]
	v_lshl_add_u64 v[50:51], v[60:61], 0, v[50:51]
	v_lshl_add_u64 v[54:55], v[60:61], 0, v[52:53]
	v_lshl_add_u64 v[62:63], v[60:61], 0, v[62:63]
	v_lshl_add_u64 v[64:65], v[60:61], 0, v[58:59]
	global_load_dwordx4 v[2:5], v[2:3], off nt
	s_nop 0
	global_load_dwordx4 v[6:9], v[6:7], off nt
	s_nop 0
	global_load_dwordx4 v[10:13], v[10:11], off nt
	s_nop 0
	global_load_dwordx4 v[14:17], v[14:15], off nt
	s_nop 0
	global_load_dwordx4 v[18:21], v[18:19], off nt
	s_nop 0
	global_load_dwordx4 v[22:25], v[22:23], off nt
	s_nop 0
	global_load_dwordx4 v[26:29], v[26:27], off nt
	s_nop 0
	global_load_dwordx4 v[30:33], v[30:31], off nt
	s_nop 0
	global_load_dwordx4 v[34:37], v[34:35], off nt
	s_nop 0
	global_load_dwordx4 v[38:41], v[38:39], off nt
	s_nop 0
	global_load_dwordx4 v[42:45], v[42:43], off nt
	s_nop 0
	global_load_dwordx4 v[46:49], v[46:47], off nt
	s_nop 0
	global_load_dwordx4 v[50:53], v[50:51], off nt
	s_nop 0
	global_load_dwordx4 v[54:57], v[54:55], off nt
	s_nop 0
	global_load_dwordx4 v[58:61], v[62:63], off nt
	s_nop 0
	global_load_dwordx4 v[62:65], v[64:65], off nt
	v_readlane_b32 s62, v255, 5
	v_readlane_b32 s63, v255, 6
	v_readlane_b32 s64, v255, 7
	v_readlane_b32 s65, v255, 8
	v_readlane_b32 s66, v255, 9
	v_readlane_b32 s67, v255, 10
	v_readlane_b32 s68, v255, 11
	v_readlane_b32 s69, v255, 12
	v_readlane_b32 s70, v255, 13
	v_readlane_b32 s71, v255, 14
	v_readlane_b32 s72, v255, 15
	v_readlane_b32 s73, v255, 16
	v_readlane_b32 s74, v255, 17
	v_readlane_b32 s75, v255, 18
	s_waitcnt vmcnt(14)
	ds_write2_b32 v106, v2, v6 offset1:4
	ds_write2_b32 v106, v3, v7 offset0:65 offset1:69
	ds_write2_b32 v106, v4, v8 offset0:130 offset1:134
	ds_write2_b32 v106, v5, v9 offset0:195 offset1:199
	s_waitcnt vmcnt(12)
	ds_write2_b32 v106, v10, v14 offset0:8 offset1:12
	ds_write2_b32 v106, v11, v15 offset0:73 offset1:77
	ds_write2_b32 v106, v12, v16 offset0:138 offset1:142
	ds_write2_b32 v106, v13, v17 offset0:203 offset1:207
	s_waitcnt vmcnt(10)
	ds_write2_b32 v106, v18, v22 offset0:16 offset1:20
	ds_write2_b32 v106, v19, v23 offset0:81 offset1:85
	ds_write2_b32 v106, v20, v24 offset0:146 offset1:150
	ds_write2_b32 v106, v21, v25 offset0:211 offset1:215
	s_waitcnt vmcnt(8)
	ds_write2_b32 v106, v26, v30 offset0:24 offset1:28
	ds_write2_b32 v106, v27, v31 offset0:89 offset1:93
	ds_write2_b32 v106, v28, v32 offset0:154 offset1:158
	ds_write2_b32 v106, v29, v33 offset0:219 offset1:223
	s_waitcnt vmcnt(6)
	ds_write2_b32 v106, v34, v38 offset0:32 offset1:36
	ds_write2_b32 v106, v35, v39 offset0:97 offset1:101
	ds_write2_b32 v106, v36, v40 offset0:162 offset1:166
	ds_write2_b32 v106, v37, v41 offset0:227 offset1:231
	s_waitcnt vmcnt(4)
	ds_write2_b32 v106, v42, v46 offset0:40 offset1:44
	ds_write2_b32 v106, v43, v47 offset0:105 offset1:109
	ds_write2_b32 v106, v44, v48 offset0:170 offset1:174
	ds_write2_b32 v106, v45, v49 offset0:235 offset1:239
	s_waitcnt vmcnt(2)
	ds_write2_b32 v106, v50, v54 offset0:48 offset1:52
	ds_write2_b32 v106, v51, v55 offset0:113 offset1:117
	ds_write2_b32 v106, v52, v56 offset0:178 offset1:182
	ds_write2_b32 v106, v53, v57 offset0:243 offset1:247
	s_waitcnt vmcnt(0)
	ds_write2_b32 v106, v58, v62 offset0:56 offset1:60
	ds_write2_b32 v106, v59, v63 offset0:121 offset1:125
	ds_write2_b32 v106, v60, v64 offset0:186 offset1:190
	ds_write2_b32 v106, v61, v65 offset0:251 offset1:255
	s_waitcnt lgkmcnt(0)
	ds_read2_b32 v[2:3], v118 offset1:1
	ds_read2_b32 v[4:5], v118 offset0:2 offset1:3
	ds_read2_b32 v[6:7], v118 offset0:4 offset1:5
	ds_read2_b32 v[8:9], v118 offset0:6 offset1:7
	v_lshl_add_u64 v[10:11], s[0:1], 1, v[96:97]
	s_waitcnt lgkmcnt(3)
	v_cvt_pk_bf16_f32 v2, v2, v3
	s_waitcnt lgkmcnt(2)
	v_cvt_pk_bf16_f32 v3, v4, v5
	s_waitcnt lgkmcnt(1)
	v_cvt_pk_bf16_f32 v4, v6, v7
	s_waitcnt lgkmcnt(0)
	v_cvt_pk_bf16_f32 v5, v8, v9
	ds_read2_b32 v[8:9], v119 offset1:1
	ds_read2_b32 v[12:13], v120 offset1:1
	ds_read2_b32 v[14:15], v121 offset1:1
	ds_read2_b32 v[16:17], v122 offset1:1
	v_or_b32_e32 v6, s2, v107
	v_lshlrev_b32_e32 v70, 11, v6
	v_lshl_add_u64 v[6:7], v[10:11], 0, v[70:71]
	global_store_dwordx4 v[6:7], v[2:5], off
	v_or_b32_e32 v6, s2, v108
	v_lshlrev_b32_e32 v70, 11, v6
	s_waitcnt lgkmcnt(0)
	v_cvt_pk_bf16_f32 v5, v16, v17
	v_add_u32_e32 v16, 0x1058, v118
	v_cvt_pk_bf16_f32 v2, v8, v9
	v_cvt_pk_bf16_f32 v3, v12, v13
	v_cvt_pk_bf16_f32 v4, v14, v15
	ds_read2_b32 v[8:9], v123 offset1:1
	ds_read2_b32 v[12:13], v124 offset1:1
	ds_read2_b32 v[14:15], v125 offset1:1
	ds_read2_b32 v[16:17], v16 offset1:1
	v_lshl_add_u64 v[6:7], v[10:11], 0, v[70:71]
	global_store_dwordx4 v[6:7], v[2:5], off
	v_or_b32_e32 v6, s2, v109
	v_lshlrev_b32_e32 v70, 11, v6
	s_waitcnt lgkmcnt(3)
	v_cvt_pk_bf16_f32 v2, v8, v9
	s_waitcnt lgkmcnt(2)
	v_cvt_pk_bf16_f32 v3, v12, v13
	s_waitcnt lgkmcnt(1)
	v_cvt_pk_bf16_f32 v4, v14, v15
	s_waitcnt lgkmcnt(0)
	v_cvt_pk_bf16_f32 v5, v16, v17
	v_add_u32_e32 v8, 0x1860, v118
	v_add_u32_e32 v12, 0x1868, v118
	v_add_u32_e32 v14, 0x1870, v118
	v_add_u32_e32 v16, 0x1878, v118
	ds_read2_b32 v[8:9], v8 offset1:1
	ds_read2_b32 v[12:13], v12 offset1:1
	ds_read2_b32 v[14:15], v14 offset1:1
	ds_read2_b32 v[16:17], v16 offset1:1
	v_lshl_add_u64 v[6:7], v[10:11], 0, v[70:71]
	global_store_dwordx4 v[6:7], v[2:5], off
	v_or_b32_e32 v6, s2, v110
	v_lshlrev_b32_e32 v70, 11, v6
	s_waitcnt lgkmcnt(3)
	v_cvt_pk_bf16_f32 v2, v8, v9
	s_waitcnt lgkmcnt(2)
	v_cvt_pk_bf16_f32 v3, v12, v13
	s_waitcnt lgkmcnt(1)
	v_cvt_pk_bf16_f32 v4, v14, v15
	s_waitcnt lgkmcnt(0)
	v_cvt_pk_bf16_f32 v5, v16, v17
	v_add_u32_e32 v8, 0x2080, v118
	v_add_u32_e32 v12, 0x2088, v118
	v_add_u32_e32 v14, 0x2090, v118
	v_add_u32_e32 v16, 0x2098, v118
	ds_read2_b32 v[8:9], v8 offset1:1
	ds_read2_b32 v[12:13], v12 offset1:1
	ds_read2_b32 v[14:15], v14 offset1:1
	ds_read2_b32 v[16:17], v16 offset1:1
	v_lshl_add_u64 v[6:7], v[10:11], 0, v[70:71]
	global_store_dwordx4 v[6:7], v[2:5], off
	v_or_b32_e32 v6, s2, v111
	v_lshlrev_b32_e32 v70, 11, v6
	s_waitcnt lgkmcnt(3)
	v_cvt_pk_bf16_f32 v2, v8, v9
	s_waitcnt lgkmcnt(2)
	v_cvt_pk_bf16_f32 v3, v12, v13
	s_waitcnt lgkmcnt(1)
	v_cvt_pk_bf16_f32 v4, v14, v15
	s_waitcnt lgkmcnt(0)
	v_cvt_pk_bf16_f32 v5, v16, v17
	v_add_u32_e32 v8, 0x28a0, v118
	v_add_u32_e32 v12, 0x28a8, v118
	v_add_u32_e32 v14, 0x28b0, v118
	v_add_u32_e32 v16, 0x28b8, v118
	ds_read2_b32 v[8:9], v8 offset1:1
	ds_read2_b32 v[12:13], v12 offset1:1
	ds_read2_b32 v[14:15], v14 offset1:1
	ds_read2_b32 v[16:17], v16 offset1:1
	v_lshl_add_u64 v[6:7], v[10:11], 0, v[70:71]
	global_store_dwordx4 v[6:7], v[2:5], off
	v_or_b32_e32 v6, s2, v112
	v_lshlrev_b32_e32 v70, 11, v6
	s_waitcnt lgkmcnt(3)
	v_cvt_pk_bf16_f32 v2, v8, v9
	s_waitcnt lgkmcnt(2)
	v_cvt_pk_bf16_f32 v3, v12, v13
	s_waitcnt lgkmcnt(1)
	v_cvt_pk_bf16_f32 v4, v14, v15
	s_waitcnt lgkmcnt(0)
	v_cvt_pk_bf16_f32 v5, v16, v17
	v_add_u32_e32 v8, 0x30c0, v118
	v_add_u32_e32 v12, 0x30c8, v118
	v_add_u32_e32 v14, 0x30d0, v118
	v_add_u32_e32 v16, 0x30d8, v118
	ds_read2_b32 v[8:9], v8 offset1:1
	ds_read2_b32 v[12:13], v12 offset1:1
	ds_read2_b32 v[14:15], v14 offset1:1
	ds_read2_b32 v[16:17], v16 offset1:1
	v_lshl_add_u64 v[6:7], v[10:11], 0, v[70:71]
	global_store_dwordx4 v[6:7], v[2:5], off
	v_or_b32_e32 v6, s2, v113
	v_lshlrev_b32_e32 v70, 11, v6
	s_waitcnt lgkmcnt(3)
	v_cvt_pk_bf16_f32 v2, v8, v9
	s_waitcnt lgkmcnt(2)
	v_cvt_pk_bf16_f32 v3, v12, v13
	s_waitcnt lgkmcnt(1)
	v_cvt_pk_bf16_f32 v4, v14, v15
	s_waitcnt lgkmcnt(0)
	v_cvt_pk_bf16_f32 v5, v16, v17
	v_add_u32_e32 v8, 0x38e0, v118
	v_add_u32_e32 v12, 0x38e8, v118
	v_add_u32_e32 v14, 0x38f0, v118
	v_add_u32_e32 v16, 0x38f8, v118
	ds_read2_b32 v[8:9], v8 offset1:1
	ds_read2_b32 v[12:13], v12 offset1:1
	ds_read2_b32 v[14:15], v14 offset1:1
	ds_read2_b32 v[16:17], v16 offset1:1
	v_lshl_add_u64 v[6:7], v[10:11], 0, v[70:71]
	global_store_dwordx4 v[6:7], v[2:5], off
	v_or_b32_e32 v6, s2, v114
	v_lshlrev_b32_e32 v70, 11, v6
	s_waitcnt lgkmcnt(3)
	v_cvt_pk_bf16_f32 v2, v8, v9
	s_waitcnt lgkmcnt(2)
	v_cvt_pk_bf16_f32 v3, v12, v13
	s_waitcnt lgkmcnt(1)
	v_cvt_pk_bf16_f32 v4, v14, v15
	s_waitcnt lgkmcnt(0)
	v_cvt_pk_bf16_f32 v5, v16, v17
	v_lshl_add_u64 v[6:7], v[10:11], 0, v[70:71]
	global_store_dwordx4 v[6:7], v[2:5], off
	s_waitcnt lgkmcnt(0)
